# V tile by LDS-DMA in both attention phases (GQA and differential)
# speedup vs baseline: 1.0229x; 1.0051x over previous
; template <int LDQ, int LDK, int LDO>
; __device__ __forceinline__ void attn_gqa16_body(const bf16* __restrict__ Qb, const bf16* __restrict__ Kh, const bf16* __restrict__ Vh, bf16* __restrict__ Ob, int seq, char* lds, float mref) {
;   const int tid = threadIdx.x, wid = tid >> 6, lane = tid & 63, l16 = lane & 15, g = lane >> 4;
;   char* V_lds = lds; char* K_lds = lds + G16_OFF_K;
;   constexpr float C = SCALE * 1.4426950408889634f; const float mnC = -mref * C;
;   float ls0 = 0.f, ls1 = 0.f; f32x4a o[8][2] = {}; bf16x8 qr[2][4];
;   { int l16q = l16, gq = g, widq = wid; asm volatile("" : "+v"(l16q), "+v"(gq), "+v"(widq));
;     const bf16* Qw = Qb + (widq >> 2) * 128 + (long)((widq & 3) * QBLK + l16q) * LDQ + gq * 8;
; #pragma unroll
;     for (int qt = 0; qt < 2; ++qt)
; #pragma unroll
;       for (int ds = 0; ds < 4; ++ds) qr[qt][ds] = *reinterpret_cast<const bf16x8*>(Qw + (long)qt * 16 * LDQ + ds * 32); }
;   const int sr = tid >> 4, sc = (tid & 15) * 8;
;   const int vst0 = (sc >> 4) * VP16 + sr * 32 + ((sc >> 3) & 1) * 16, vst1 = vst0 + 1024;
;   const int vb0 = (int)(uintptr_t)V_lds + (4 * g + (l16 >> 2)) * 32 + (l16 & 3) * 8;
;   const int kb0 = l16 * 272 + g * 16;
;   bf16x8 sv0, sv1, sk0, sk1;
;   const unsigned koff0 = (unsigned)(sr * LDK + sc) * 2u, koff1 = koff0 + 32u * LDK * 2u;
.LBB0_638:
	s_andn2_saveexec_b64 s[6:7], s[30:31]
	s_cbranch_execz .LBB0_652
	s_and_b64 vcc, exec, s[4:5]
	s_cbranch_vccnz .LBB0_652
	v_lshrrev_b32_e32 v3, 4, v5
	v_lshlrev_b32_e32 v5, 5, v1
	s_movk_i32 s0, 0x820
	v_mad_u32_u24 v3, v3, s0, v5
	v_and_b32_e32 v180, 15, v0
	v_and_or_b32 v3, v4, 16, v3
	v_lshlrev_b32_e32 v8, 3, v0
	v_lshlrev_b32_e32 v6, 4, v176
	v_add_u32_e32 v181, 0, v3
	v_mul_u32_u24_e32 v3, 0x110, v180
	s_cmp_lg_u32 0, -1
	v_add3_u32 v182, 0, v6, v3
	v_and_b32_e32 v3, 0x60, v8
	s_cselect_b32 s0, 0, 0
	v_add_u32_e32 v3, s0, v3
	s_movk_i32 s0, 0xff
	v_cmp_lt_u32_e64 s[4:5], s0, v0
	s_add_u32 s0, s28, 0x3f552400
	s_addc_u32 s1, s29, 0
	s_add_u32 s2, s28, 0x3f552c00
	s_addc_u32 s18, s29, 0
	s_add_u32 s19, s28, 0x3f552e00
	s_addc_u32 s20, s29, 0
	s_add_u32 s21, s28, 0x36552c00
	v_lshlrev_b32_e32 v4, 7, v176
	v_and_b32_e32 v5, 24, v8
	s_addc_u32 s22, s29, 0
	v_lshlrev_b32_e32 v2, 1, v2
	v_add3_u32 v183, v3, v5, v4
	s_add_u32 s23, s28, 0x36552e00
	v_lshl_add_u32 v2, v180, 4, v2
	v_mov_b32_e32 v3, 0
	s_mov_b32 s9, 0
	v_add_u32_e32 v184, 0x4100, v183
	v_lshrrev_b32_e32 v185, 6, v0
	v_mul_f32_e32 v186, 0xbe0293ee, v7
	s_addc_u32 s24, s29, 0
	v_lshl_add_u64 v[154:155], s[28:29], 0, v[2:3]
	s_mov_b32 s25, 0x120000
	s_movk_i32 s26, 0x2400
	s_mov_b32 s27, 0x24000
	s_mov_b32 s28, 0x48000
	s_mov_b32 s29, 0x90000
	s_mov_b32 s30, 0xd8000
	s_mov_b32 s31, 0x168000
	s_mov_b32 s34, 0x1b0000
	s_mov_b32 s36, 0x1f8000
	s_mov_b32 s37, 0x36702000
	s_mov_b32 s38, 0x3674a000
	s_mov_b32 s39, 0x36672000
	s_mov_b32 s40, 0x366ba000
	s_movk_i32 s41, 0x7fff
	s_mov_b32 s44, 0x10000
	v_mov_b32_e32 v187, 1
	s_mov_b32 s45, s94
	v_and_b32_e32 v253, 63, v0
	v_lshrrev_b32_e32 v252, 1, v253
	v_mul_u32_u24_e32 v252, 0x2400, v252
	v_and_b32_e32 v253, 1, v253
	v_lshl_add_u32 v252, v253, 4, v252
	v_lshrrev_b32_e32 v253, 6, v0
	v_lshl_add_u32 v253, v253, 5, v252
	v_lshrrev_b32_e32 v252, 6, v0
	v_mul_u32_u24_e32 v252, 0x820, v252
	s_nop 0
	v_readfirstlane_b32 s84, v252
	s_nop 3
	s_add_i32 s86, s84, 0x4100
	s_branch .LBB0_642

; #define HLOADV(kt) do { const char* vb_ = (const char*)Vh + (size_t)(kt) * (64 * LDK * 2); sv0 = *(const bf16x8*)(vb_ + koff0); sv1 = *(const bf16x8*)(vb_ + koff1); } while (0)
; #define HLOADK(kt) do { const char* kb_ = (const char*)Kh + (size_t)(kt) * (64 * LDK * 2); sk0 = *(const bf16x8*)(kb_ + koff0); sk1 = *(const bf16x8*)(kb_ + koff1); } while (0)
; #define HWRITEV(b) do { char* d_ = V_lds + (b) * G16_V; *(bf16x8*)(d_ + vst0) = sv0; *(bf16x8*)(d_ + vst1) = sv1; } while (0)
; #define HWRITEK(b) do { char* d_ = K_lds + (b) * GB_K; *(bf16x8*)(d_ + KSWZ(sr, sc * 2)) = sk0; *(bf16x8*)(d_ + KSWZ(32 + sr, sc * 2)) = sk1; } while (0)
; #define HEXP() do { _Pragma("unroll") for (int kt = 0; kt < 4; ++kt) { _Pragma("unroll") for (int qt = 0; qt < 2; ++qt) { _Pragma("unroll") for (int i = 0; i < 4; ++i) s[kt][qt][i] = __builtin_amdgcn_exp2f(fmaf(s[kt][qt][i], C, mnC)); } } } while (0)
; template <int LDQ, int LDK, int LDO>
; __device__ __forceinline__ void attn_gqa16_body(const bf16* __restrict__ Qb, const bf16* __restrict__ Kh, const bf16* __restrict__ Vh, bf16* __restrict__ Ob, int seq, char* lds, float mref) {
;     ...
;   { int l16q = l16, gq = g, widq = wid; asm volatile("" : "+v"(l16q), "+v"(gq), "+v"(widq));
;     const bf16* Qw = Qb + (widq >> 2) * 128 + (long)((widq & 3) * QBLK + l16q) * LDQ + gq * 8;
; #pragma unroll
;     for (int qt = 0; qt < 2; ++qt)
; #pragma unroll
;       for (int ds = 0; ds < 4; ++ds) qr[qt][ds] = *reinterpret_cast<const bf16x8*>(Qw + (long)qt * 16 * LDQ + ds * 32); }
;   const int sr = tid >> 4, sc = (tid & 15) * 8;
;   const int vst0 = (sc >> 4) * VP16 + sr * 32 + ((sc >> 3) & 1) * 16, vst1 = vst0 + 1024;
;   const int vb0 = (int)(uintptr_t)V_lds + (4 * g + (l16 >> 2)) * 32 + (l16 & 3) * 8;
;   const int kb0 = l16 * 272 + g * 16;
;   bf16x8 sv0, sv1, sk0, sk1;
;   const unsigned koff0 = (unsigned)(sr * LDK + sc) * 2u, koff1 = koff0 + 32u * LDK * 2u;
;     ...
;   f32x4a s[4][2]; bf16x8 pb[2][2];
;     ...
;   const int NT = seq / KVBLK;
;   HLOADK(0); HLOADV(0); asm volatile("s_waitcnt vmcnt(0)" ::: "memory"); HWRITEK(0); HWRITEV(0);
;   HLOADK(1); asm volatile("s_waitcnt vmcnt(0)" ::: "memory"); HWRITEK(1); __syncthreads();
;   HLOADK(2); HLOADV(1);
;   HQK(0); HEXP();
.LBB0_646:
	s_and_b64 vcc, exec, s[14:15]
	s_cbranch_vccz .LBB0_641
	s_lshl_b32 s8, s45, 7
	s_and_b32 s8, s8, 0x3f80
	s_ashr_i32 s14, s45, 8
	s_mul_i32 s12, s8, 0x2400
	s_add_u32 s15, s33, s12
	s_addc_u32 s17, s35, 0
	s_lshl_b32 s13, s45, 1
	s_lshl_b32 s12, s14, 9
	s_and_b32 s13, s13, 0x100
	s_or_b32 s12, s12, s13
	s_ashr_i32 s13, s12, 31
	v_mov_b32_e32 v4, v180
	v_mov_b32_e32 v2, v185
	v_mov_b32_e32 v5, v176
	s_lshl_b64 s[12:13], s[12:13], 1
	s_add_u32 s16, s15, s12
	v_lshlrev_b32_e32 v6, 5, v2
	v_and_b32_e32 v2, 0xffffff80, v6
	s_addc_u32 s17, s17, s13
	v_ashrrev_i32_e32 v3, 31, v2
	v_and_b32_e32 v6, 0x60, v6
	s_lshl_b32 s14, s14, 7
	v_lshl_add_u64 v[2:3], v[2:3], 1, s[16:17]
	v_add_u32_e32 v4, v6, v4
	s_ashr_i32 s15, s14, 31
	v_mad_i64_i32 v[2:3], s[16:17], v4, s26, v[2:3]
	v_lshlrev_b32_e32 v4, 3, v5
	s_lshl_b64 s[46:47], s[14:15], 1
	v_ashrrev_i32_e32 v5, 31, v4
	s_add_u32 s48, s21, s46
	v_lshl_add_u64 v[6:7], v[4:5], 1, v[2:3]
	s_addc_u32 s49, s22, s47
	global_load_dwordx4 v[30:33], v[6:7], off
	global_load_dwordx4 v[18:21], v[6:7], off offset:64
	global_load_dwordx4 v[10:13], v[6:7], off offset:128
	global_load_dwordx4 v[2:5], v[6:7], off offset:192
	v_add_co_u32_e32 v6, vcc, s27, v6
	s_add_u32 s46, s23, s46
	s_nop 0
	v_addc_co_u32_e32 v7, vcc, 0, v7, vcc
	v_lshl_add_u64 v[102:103], s[48:49], 0, v[178:179]
	s_addc_u32 s47, s24, s47
	s_add_u32 s74, s46, 0x90000
	s_addc_u32 s75, s47, 0
	s_add_u32 s76, s74, 0x48000
	s_addc_u32 s77, s75, 0
	v_add_co_u32_e32 v34, vcc, s28, v102
	v_lshl_add_u64 v[104:105], s[46:47], 0, v[178:179]
	s_nop 0
	v_addc_co_u32_e32 v35, vcc, 0, v103, vcc
	v_add_co_u32_e32 v46, vcc, s28, v104
	global_load_dwordx4 v[38:41], v[6:7], off
	global_load_dwordx4 v[22:25], v[6:7], off offset:64
	global_load_dwordx4 v[14:17], v[6:7], off offset:128
	s_nop 0
	global_load_dwordx4 v[6:9], v[6:7], off offset:192
	v_addc_co_u32_e32 v47, vcc, 0, v105, vcc
	v_add_co_u32_e32 v50, vcc, s29, v102
	global_load_dwordx4 v[26:29], v[102:103], off
	s_nop 0
	global_load_dwordx4 v[34:37], v[34:35], off
	v_addc_co_u32_e32 v51, vcc, 0, v103, vcc
	v_add_co_u32_e32 v54, vcc, s30, v102
	global_load_dwordx4 v[42:45], v[104:105], off
	s_nop 0
	global_load_dwordx4 v[46:49], v[46:47], off
	s_waitcnt vmcnt(0)
	v_addc_co_u32_e32 v55, vcc, 0, v103, vcc
	global_load_dwordx4 v[50:53], v[50:51], off
	s_nop 0
	global_load_dwordx4 v[54:57], v[54:55], off
	s_waitcnt vmcnt(5)
	ds_write_b128 v194, v[26:29] offset:33280
	s_waitcnt vmcnt(4)
	ds_write_b128 v194, v[34:37] offset:41984
	s_waitcnt vmcnt(3)
	ds_write_b128 v181, v[42:45]
	s_waitcnt vmcnt(2)
	ds_write_b128 v181, v[46:49] offset:1024
	s_waitcnt vmcnt(0)
	s_waitcnt vmcnt(1)
	ds_write_b128 v194, v[50:53] offset:50688
	s_waitcnt vmcnt(0)
	ds_write_b128 v194, v[54:57] offset:59392
	s_waitcnt lgkmcnt(0)
	s_barrier
	ds_read_b128 v[26:29], v182 offset:33280
	ds_read_b128 v[34:37], v182 offset:33344
	ds_read_b128 v[46:49], v182 offset:37632
	ds_read_b128 v[50:53], v182 offset:37696
	ds_read_b128 v[58:61], v182 offset:41984
	ds_read_b128 v[62:65], v182 offset:42048
	ds_read_b128 v[70:73], v182 offset:46336
	ds_read_b128 v[74:77], v182 offset:46400
	s_waitcnt lgkmcnt(7)
	v_mfma_f32_16x16x32_bf16 v[42:45], v[26:29], v[30:33], 0
	v_mfma_f32_16x16x32_bf16 v[26:29], v[26:29], v[38:41], 0
	s_waitcnt lgkmcnt(5)
	v_mfma_f32_16x16x32_bf16 v[54:57], v[46:49], v[30:33], 0
	v_mfma_f32_16x16x32_bf16 v[46:49], v[46:49], v[38:41], 0
	s_waitcnt lgkmcnt(3)
	v_mfma_f32_16x16x32_bf16 v[66:69], v[58:61], v[30:33], 0
	v_mfma_f32_16x16x32_bf16 v[58:61], v[58:61], v[38:41], 0
	s_waitcnt lgkmcnt(1)
	v_mfma_f32_16x16x32_bf16 v[78:81], v[70:73], v[30:33], 0
	v_mfma_f32_16x16x32_bf16 v[70:73], v[70:73], v[38:41], 0
	v_mfma_f32_16x16x32_bf16 v[42:45], v[34:37], v[18:21], v[42:45]
	v_mfma_f32_16x16x32_bf16 v[26:29], v[34:37], v[22:25], v[26:29]
	v_mfma_f32_16x16x32_bf16 v[34:37], v[50:53], v[18:21], v[54:57]
	v_mfma_f32_16x16x32_bf16 v[46:49], v[50:53], v[22:25], v[46:49]
	v_mfma_f32_16x16x32_bf16 v[50:53], v[62:65], v[18:21], v[66:69]
	v_mfma_f32_16x16x32_bf16 v[54:57], v[62:65], v[22:25], v[58:61]
	s_waitcnt lgkmcnt(0)
	v_mfma_f32_16x16x32_bf16 v[58:61], v[74:77], v[18:21], v[78:81]
	v_mfma_f32_16x16x32_bf16 v[62:65], v[74:77], v[22:25], v[70:73]
	ds_read_b128 v[66:69], v182 offset:33408
	ds_read_b128 v[74:77], v182 offset:33472
	s_waitcnt lgkmcnt(1)
	v_mfma_f32_16x16x32_bf16 v[42:45], v[66:69], v[10:13], v[42:45]
	v_mfma_f32_16x16x32_bf16 v[26:29], v[66:69], v[14:17], v[26:29]
	ds_read_b128 v[66:69], v182 offset:37760
	ds_read_b128 v[78:81], v182 offset:37824
	s_waitcnt lgkmcnt(1)
	v_mfma_f32_16x16x32_bf16 v[34:37], v[66:69], v[10:13], v[34:37]
	v_mfma_f32_16x16x32_bf16 v[46:49], v[66:69], v[14:17], v[46:49]
	ds_read_b128 v[66:69], v182 offset:42112
	ds_read_b128 v[82:85], v182 offset:42176
	s_waitcnt lgkmcnt(1)
	v_mfma_f32_16x16x32_bf16 v[50:53], v[66:69], v[10:13], v[50:53]
	v_mfma_f32_16x16x32_bf16 v[86:89], v[66:69], v[14:17], v[54:57]
	s_nop 2
	ds_read_b128 v[54:57], v182 offset:46464
	ds_read_b128 v[90:93], v182 offset:46528
	v_mfma_f32_16x16x32_bf16 v[66:69], v[74:77], v[6:9], v[26:29]
	s_nop 2
	v_add_co_u32_e32 v26, vcc, s25, v102
	s_waitcnt lgkmcnt(1)
	v_mfma_f32_16x16x32_bf16 v[98:101], v[54:57], v[14:17], v[62:65]
	v_addc_co_u32_e32 v27, vcc, 0, v103, vcc
	v_add_co_u32_e32 v28, vcc, s31, v102
	v_mfma_f32_16x16x32_bf16 v[62:65], v[78:81], v[2:5], v[34:37]
	s_nop 0
	v_addc_co_u32_e32 v29, vcc, 0, v103, vcc
	global_load_dwordx4 v[106:109], v[26:27], off
	global_load_dwordx4 v[110:113], v[28:29], off
	v_add_co_u32_e32 v26, vcc, s29, v104
	v_mfma_f32_16x16x32_bf16 v[94:97], v[54:57], v[10:13], v[58:61]
	s_nop 0
	v_addc_co_u32_e32 v27, vcc, 0, v105, vcc
	v_add_co_u32_e32 v34, vcc, s30, v104
	v_mfma_f32_16x16x32_bf16 v[70:73], v[74:77], v[2:5], v[42:45]
	s_nop 0
	v_addc_co_u32_e32 v35, vcc, 0, v105, vcc
	s_nop 0
	v_mfma_f32_16x16x32_bf16 v[58:61], v[78:81], v[6:9], v[46:49]
	v_mfma_f32_16x16x32_bf16 v[54:57], v[82:85], v[2:5], v[50:53]
	v_mfma_f32_16x16x32_bf16 v[50:53], v[82:85], v[6:9], v[86:89]
	s_waitcnt lgkmcnt(0)
; #define HLOADV(kt) do { const char* vb_ = (const char*)Vh + (size_t)(kt) * (64 * LDK * 2); sv0 = *(const bf16x8*)(vb_ + koff0); sv1 = *(const bf16x8*)(vb_ + koff1); } while (0)
; #define HLOADK(kt) do { const char* kb_ = (const char*)Kh + (size_t)(kt) * (64 * LDK * 2); sk0 = *(const bf16x8*)(kb_ + koff0); sk1 = *(const bf16x8*)(kb_ + koff1); } while (0)
; #define HWRITEV(b) do { char* d_ = V_lds + (b) * G16_V; *(bf16x8*)(d_ + vst0) = sv0; *(bf16x8*)(d_ + vst1) = sv1; } while (0)
; #define HWRITEK(b) do { char* d_ = K_lds + (b) * GB_K; *(bf16x8*)(d_ + KSWZ(sr, sc * 2)) = sk0; *(bf16x8*)(d_ + KSWZ(32 + sr, sc * 2)) = sk1; } while (0)
; #define HEXP() do { _Pragma("unroll") for (int kt = 0; kt < 4; ++kt) { _Pragma("unroll") for (int qt = 0; qt < 2; ++qt) { _Pragma("unroll") for (int i = 0; i < 4; ++i) s[kt][qt][i] = __builtin_amdgcn_exp2f(fmaf(s[kt][qt][i], C, mnC)); } } } while (0)
; template <int LDQ, int LDK, int LDO>
; __device__ __forceinline__ void attn_gqa16_body(const bf16* __restrict__ Qb, const bf16* __restrict__ Kh, const bf16* __restrict__ Vh, bf16* __restrict__ Ob, int seq, char* lds, float mref) {
;     ...
;   const int NT = seq / KVBLK;
;   HLOADK(0); HLOADV(0); asm volatile("s_waitcnt vmcnt(0)" ::: "memory"); HWRITEK(0); HWRITEV(0);
;   HLOADK(1); asm volatile("s_waitcnt vmcnt(0)" ::: "memory"); HWRITEK(1); __syncthreads();
;   HLOADK(2); HLOADV(1);
;   HQK(0); HEXP();
;   if (wid >= 4) __builtin_amdgcn_s_setprio(1);
;   for (int t = 0; t < NT; ++t) {
;     HPACK();
;     __syncthreads();
	v_mfma_f32_16x16x32_bf16 v[46:49], v[90:93], v[2:5], v[94:97]
	v_mfma_f32_16x16x32_bf16 v[42:45], v[90:93], v[6:9], v[98:101]
	s_and_saveexec_b64 s[16:17], s[4:5]
	s_setprio 1
	s_or_b64 exec, exec, s[16:17]
	v_fmamk_f32 v70, v70, 0x3e0293ee, v186
	v_fmamk_f32 v66, v66, 0x3e0293ee, v186
	v_fmamk_f32 v62, v62, 0x3e0293ee, v186
	v_fmamk_f32 v58, v58, 0x3e0293ee, v186
	v_fmamk_f32 v54, v54, 0x3e0293ee, v186
	v_fmamk_f32 v50, v50, 0x3e0293ee, v186
	v_fmamk_f32 v46, v46, 0x3e0293ee, v186
	v_fmamk_f32 v42, v42, 0x3e0293ee, v186
	v_exp_f32_e32 v158, v70
	v_fmamk_f32 v70, v71, 0x3e0293ee, v186
	v_exp_f32_e32 v159, v66
	v_fmamk_f32 v66, v67, 0x3e0293ee, v186
	v_exp_f32_e32 v168, v62
	v_fmamk_f32 v62, v63, 0x3e0293ee, v186
	v_exp_f32_e32 v169, v58
	v_fmamk_f32 v58, v59, 0x3e0293ee, v186
	v_exp_f32_e32 v142, v54
	v_fmamk_f32 v54, v55, 0x3e0293ee, v186
	v_exp_f32_e32 v143, v50
	v_fmamk_f32 v50, v51, 0x3e0293ee, v186
	v_exp_f32_e32 v134, v46
	v_fmamk_f32 v46, v47, 0x3e0293ee, v186
	v_exp_f32_e32 v135, v42
	v_fmamk_f32 v42, v43, 0x3e0293ee, v186
	v_exp_f32_e32 v152, v70
	v_fmamk_f32 v70, v72, 0x3e0293ee, v186
	v_exp_f32_e32 v153, v66
	v_fmamk_f32 v66, v68, 0x3e0293ee, v186
	v_exp_f32_e32 v170, v62
	v_fmamk_f32 v62, v64, 0x3e0293ee, v186
	v_exp_f32_e32 v171, v58
	v_fmamk_f32 v58, v60, 0x3e0293ee, v186
	v_exp_f32_e32 v172, v54
	v_fmamk_f32 v54, v56, 0x3e0293ee, v186
	v_exp_f32_e32 v173, v50
	v_fmamk_f32 v50, v52, 0x3e0293ee, v186
	v_exp_f32_e32 v138, v46
	v_fmamk_f32 v46, v48, 0x3e0293ee, v186
	v_exp_f32_e32 v139, v42
	v_fmamk_f32 v42, v44, 0x3e0293ee, v186
	v_exp_f32_e32 v156, v70
	v_fmamk_f32 v70, v73, 0x3e0293ee, v186
	v_exp_f32_e32 v157, v66
	v_fmamk_f32 v66, v69, 0x3e0293ee, v186
	v_exp_f32_e32 v164, v62
	v_fmamk_f32 v62, v65, 0x3e0293ee, v186
	v_exp_f32_e32 v165, v58
	v_fmamk_f32 v58, v61, 0x3e0293ee, v186
	v_exp_f32_e32 v144, v54
	v_fmamk_f32 v54, v57, 0x3e0293ee, v186
	v_exp_f32_e32 v145, v50
	v_fmamk_f32 v50, v53, 0x3e0293ee, v186
	v_exp_f32_e32 v136, v46
	v_fmamk_f32 v46, v49, 0x3e0293ee, v186
	v_exp_f32_e32 v137, v42
	v_fmamk_f32 v42, v45, 0x3e0293ee, v186
	v_exp_f32_e32 v160, v70
	v_exp_f32_e32 v161, v66
	v_exp_f32_e32 v166, v62
	v_exp_f32_e32 v167, v58
	v_exp_f32_e32 v174, v54
	v_exp_f32_e32 v175, v50
	v_exp_f32_e32 v140, v46
	v_exp_f32_e32 v141, v42
	v_mov_b32_e32 v50, 0
	v_lshl_add_u64 v[162:163], s[14:15], 1, v[154:155]
	s_mov_b32 s16, 0
	s_mov_b64 s[14:15], 0
	v_mov_b32_e32 v51, v50
	v_mov_b32_e32 v52, v50
	v_mov_b32_e32 v53, v50
	v_mov_b32_e32 v78, v50
	v_mov_b32_e32 v79, v50
	v_mov_b32_e32 v80, v50
	v_mov_b32_e32 v81, v50
	v_mov_b32_e32 v90, v50
	v_mov_b32_e32 v91, v50
	v_mov_b32_e32 v92, v50
	v_mov_b32_e32 v93, v50
	v_mov_b32_e32 v94, v50
	v_mov_b32_e32 v95, v50
	v_mov_b32_e32 v96, v50
	v_mov_b32_e32 v97, v50
	v_mov_b32_e32 v98, v50
	v_mov_b32_e32 v99, v50
	v_mov_b32_e32 v100, v50
	v_mov_b32_e32 v101, v50
	v_mov_b32_e32 v102, v50
	v_mov_b32_e32 v103, v50
	v_mov_b32_e32 v104, v50
	v_mov_b32_e32 v105, v50
	v_mov_b32_e32 v82, v50
	v_mov_b32_e32 v83, v50
	v_mov_b32_e32 v84, v50
	v_mov_b32_e32 v85, v50
	v_mov_b32_e32 v86, v50
	v_mov_b32_e32 v87, v50
	v_mov_b32_e32 v88, v50
	v_mov_b32_e32 v89, v50
	v_mov_b32_e32 v54, v50
	v_mov_b32_e32 v55, v50
	v_mov_b32_e32 v56, v50
	v_mov_b32_e32 v57, v50
	v_mov_b32_e32 v62, v50
	v_mov_b32_e32 v63, v50
	v_mov_b32_e32 v64, v50
	v_mov_b32_e32 v65, v50
	v_mov_b32_e32 v58, v50
	v_mov_b32_e32 v59, v50
	v_mov_b32_e32 v60, v50
	v_mov_b32_e32 v61, v50
	v_mov_b32_e32 v70, v50
	v_mov_b32_e32 v71, v50
	v_mov_b32_e32 v72, v50
	v_mov_b32_e32 v73, v50
	v_mov_b32_e32 v42, v50
	v_mov_b32_e32 v43, v50
	v_mov_b32_e32 v44, v50
	v_mov_b32_e32 v45, v50
	v_mov_b32_e32 v46, v50
	v_mov_b32_e32 v47, v50
	v_mov_b32_e32 v48, v50
	v_mov_b32_e32 v49, v50
	v_mov_b32_e32 v66, v50
	v_mov_b32_e32 v67, v50
	v_mov_b32_e32 v68, v50
	v_mov_b32_e32 v69, v50
	v_mov_b32_e32 v74, v50
	v_mov_b32_e32 v75, v50
	v_mov_b32_e32 v76, v50
	v_mov_b32_e32 v77, v50
	v_mov_b32_e32 v150, v50
	v_mov_b32_e32 v151, v50
.LBB0_650:
	s_add_i32 s17, s16, 1
	s_and_b32 s16, s16, 1
	s_and_b32 s46, 1, s17
	s_cmp_eq_u32 s46, 1
	s_cselect_b32 s85, s86, s84
	s_cselect_b32 s46, 0x4400, 0
	v_add_u32_e32 v189, s46, v182
	v_cvt_pk_bf16_f32 v114, v158, v152
	v_cvt_pk_bf16_f32 v115, v156, v160
	v_cvt_pk_bf16_f32 v116, v168, v170
	v_cvt_pk_bf16_f32 v117, v164, v166
	v_cvt_pk_bf16_f32 v118, v159, v153
	v_cvt_pk_bf16_f32 v119, v157, v161
	v_cvt_pk_bf16_f32 v120, v169, v171
	v_cvt_pk_bf16_f32 v121, v165, v167
	v_cvt_pk_bf16_f32 v122, v142, v172
	v_cvt_pk_bf16_f32 v123, v144, v174
	v_cvt_pk_bf16_f32 v124, v134, v138
	v_cvt_pk_bf16_f32 v125, v136, v140
	v_cvt_pk_bf16_f32 v126, v143, v173
	v_cvt_pk_bf16_f32 v127, v145, v175
	v_cvt_pk_bf16_f32 v128, v135, v139
	v_cvt_pk_bf16_f32 v129, v137, v141
	s_waitcnt vmcnt(2)
	s_barrier
; #define SBAR() __builtin_amdgcn_sched_barrier(0)
; #define MFMA16(a, b, c) __builtin_amdgcn_mfma_f32_16x16x32_bf16(a, b, c, 0, 0, 0)
; template <int D0> __device__ __forceinline__ void pv16(f32x4a (&o)[8][2], int vb, const bf16x8 (&pb)[2][2]) {
;     ...
;   const s16x4 a0 = TR(D0, 0, 0), a1 = TR(D0, 0, 1), a2 = TR(D0, 1, 0), a3 = TR(D0, 1, 1), b0 = TR(D0 + 1, 0, 0), b1 = TR(D0 + 1, 0, 1), b2 = TR(D0 + 1, 1, 0), b3 = TR(D0 + 1, 1, 1);
;   const s16x4 c0 = TR(D0 + 2, 0, 0), c1 = TR(D0 + 2, 0, 1), c2 = TR(D0 + 2, 1, 0), c3 = TR(D0 + 2, 1, 1);
;   asm volatile("s_waitcnt lgkmcnt(4)" ::: "memory"); SBAR();
;   o[D0][0] = MFMA16(PK16(a0, a1), pb[0][0], o[D0][0]); o[D0][1] = MFMA16(PK16(a0, a1), pb[0][1], o[D0][1]);
;   o[D0 + 1][0] = MFMA16(PK16(b0, b1), pb[0][0], o[D0 + 1][0]); o[D0 + 1][1] = MFMA16(PK16(b0, b1), pb[0][1], o[D0 + 1][1]);
;   o[D0][0] = MFMA16(PK16(a2, a3), pb[1][0], o[D0][0]); o[D0][1] = MFMA16(PK16(a2, a3), pb[1][1], o[D0][1]);
;   o[D0 + 1][0] = MFMA16(PK16(b2, b3), pb[1][0], o[D0 + 1][0]); o[D0 + 1][1] = MFMA16(PK16(b2, b3), pb[1][1], o[D0 + 1][1]);
;   SBAR();
; template <int LDQ, int LDK, int LDO>
; __device__ __forceinline__ void attn_gqa16_body(const bf16* __restrict__ Qb, const bf16* __restrict__ Kh, const bf16* __restrict__ Vh, bf16* __restrict__ Ob, int seq, char* lds, float mref) {
;     ...
;     HPACK();
;     __syncthreads();
;     const bool more = t + 1 < NT;
;     if (more) HQK((t + 1) & 1);
;     const int vb = vb0 + (t & 1) * (int)G16_V;
;     SBAR(); pv16<0>(o, vb, pb); SBAR();
	ds_read_b128 v[130:133], v189 offset:33280
	ds_read_b128 v[146:149], v189 offset:33344
	ds_read_b128 v[200:203], v189 offset:37632
	ds_read_b128 v[204:207], v189 offset:37696
	ds_read_b128 v[212:215], v189 offset:41984
	ds_read_b128 v[216:219], v189 offset:42048
	ds_read_b128 v[224:227], v189 offset:46336
	ds_read_b128 v[228:231], v189 offset:46400
	s_mov_b32 m0, s85
	s_nop 0
	global_load_lds_dwordx4 v253, s[74:75]
	s_add_i32 m0, s85, 0x400
	s_nop 0
	global_load_lds_dwordx4 v253, s[76:77]
	s_add_u32 s74, s74, 0x90000
	s_addc_u32 s75, s75, 0
	s_add_u32 s76, s76, 0x90000
	s_addc_u32 s77, s77, 0
	s_waitcnt lgkmcnt(7)
	v_mfma_f32_16x16x32_bf16 v[196:199], v[130:133], v[30:33], 0
	v_add_f32_e64 v134, v134, v138
	v_add_f32_e64 v135, v135, v139
	v_pk_add_f32 v[136:137], v[136:137], v[140:141]
	s_mul_i32 s46, s16, 0x4100
	v_mfma_f32_16x16x32_bf16 v[130:133], v[130:133], v[38:41], 0
	s_waitcnt lgkmcnt(5)
	v_mfma_f32_16x16x32_bf16 v[208:211], v[200:203], v[30:33], 0
	v_mfma_f32_16x16x32_bf16 v[200:203], v[200:203], v[38:41], 0
	s_waitcnt lgkmcnt(3)
	v_mfma_f32_16x16x32_bf16 v[220:223], v[212:215], v[30:33], 0
	v_mfma_f32_16x16x32_bf16 v[212:215], v[212:215], v[38:41], 0
	s_waitcnt lgkmcnt(1)
	v_mfma_f32_16x16x32_bf16 v[232:235], v[224:227], v[30:33], 0
	v_mfma_f32_16x16x32_bf16 v[224:227], v[224:227], v[38:41], 0
	v_mfma_f32_16x16x32_bf16 v[196:199], v[146:149], v[18:21], v[196:199]
	v_mfma_f32_16x16x32_bf16 v[130:133], v[146:149], v[22:25], v[130:133]
	v_mfma_f32_16x16x32_bf16 v[146:149], v[204:207], v[18:21], v[208:211]
	v_mfma_f32_16x16x32_bf16 v[200:203], v[204:207], v[22:25], v[200:203]
	v_mfma_f32_16x16x32_bf16 v[204:207], v[216:219], v[18:21], v[220:223]
	v_mfma_f32_16x16x32_bf16 v[208:211], v[216:219], v[22:25], v[212:215]
	s_waitcnt lgkmcnt(0)
	v_mfma_f32_16x16x32_bf16 v[216:219], v[228:231], v[22:25], v[224:227]
	ds_read_b128 v[220:223], v189 offset:33408
	s_nop 1
	ds_read_b128 v[224:227], v189 offset:33472
	v_mfma_f32_16x16x32_bf16 v[212:215], v[228:231], v[18:21], v[232:235]
	s_waitcnt lgkmcnt(1)
	v_mfma_f32_16x16x32_bf16 v[196:199], v[220:223], v[10:13], v[196:199]
	v_mfma_f32_16x16x32_bf16 v[130:133], v[220:223], v[14:17], v[130:133]
	ds_read_b128 v[220:223], v189 offset:37760
	ds_read_b128 v[228:231], v189 offset:37824
	s_waitcnt lgkmcnt(1)
	v_mfma_f32_16x16x32_bf16 v[146:149], v[220:223], v[10:13], v[146:149]
	v_mfma_f32_16x16x32_bf16 v[200:203], v[220:223], v[14:17], v[200:203]
	ds_read_b128 v[220:223], v189 offset:42112
	ds_read_b128 v[232:235], v189 offset:42176
	s_waitcnt lgkmcnt(1)
	v_mfma_f32_16x16x32_bf16 v[204:207], v[220:223], v[10:13], v[204:207]
	v_mfma_f32_16x16x32_bf16 v[208:211], v[220:223], v[14:17], v[208:211]
	ds_read_b128 v[220:223], v189 offset:46464
	ds_read_b128 v[236:239], v189 offset:46528
	v_add_u32_e32 v189, s46, v183
	s_waitcnt lgkmcnt(1)
	v_mfma_f32_16x16x32_bf16 v[212:215], v[220:223], v[10:13], v[212:215]
	v_mfma_f32_16x16x32_bf16 v[216:219], v[220:223], v[14:17], v[216:219]
	v_mfma_f32_16x16x32_bf16 v[220:223], v[224:227], v[6:9], v[130:133]
	s_nop 2
	v_add_f32_e64 v130, v158, v152
	v_add_f32_e64 v131, v159, v153
	v_pk_add_f32 v[132:133], v[156:157], v[160:161]
	v_pk_add_f32 v[152:153], v[168:169], v[170:171]
	v_pk_add_f32 v[156:157], v[164:165], v[166:167]
	v_pk_add_f32 v[158:159], v[142:143], v[172:173]
	v_pk_add_f32 v[160:161], v[144:145], v[174:175]
	v_pk_add_f32 v[130:131], v[130:131], v[132:133]
	v_mfma_f32_16x16x32_bf16 v[142:145], v[232:235], v[2:5], v[204:207]
	v_add_f32_e64 v152, v152, v156
	v_add_f32_e64 v153, v153, v157
	v_pk_add_f32 v[156:157], v[158:159], v[160:161]
	v_pk_add_f32 v[158:159], v[134:135], v[136:137]
	v_mfma_f32_16x16x32_bf16 v[138:141], v[232:235], v[6:9], v[208:211]
	v_add_f32_e64 v150, v150, v130
	v_add_f32_e64 v151, v151, v131
	v_pk_add_f32 v[150:151], v[152:153], v[150:151]
	s_waitcnt lgkmcnt(0)
	v_mfma_f32_16x16x32_bf16 v[134:137], v[236:239], v[2:5], v[212:215]
	v_add_f32_e64 v150, v156, v150
	v_add_f32_e64 v151, v157, v151
	v_pk_add_f32 v[150:151], v[158:159], v[150:151]
	v_mfma_f32_16x16x32_bf16 v[196:199], v[224:227], v[2:5], v[196:199]
	v_mfma_f32_16x16x32_bf16 v[224:227], v[228:231], v[2:5], v[146:149]
	v_mfma_f32_16x16x32_bf16 v[146:149], v[228:231], v[6:9], v[200:203]
	v_mfma_f32_16x16x32_bf16 v[130:133], v[236:239], v[6:9], v[216:219]
	ds_read_b64_tr_b16 v[156:157], v189 offset:0
	ds_read_b64_tr_b16 v[158:159], v189 offset:0x200
	ds_read_b64_tr_b16 v[164:165], v189 offset:0x400
	ds_read_b64_tr_b16 v[166:167], v189 offset:0x600
	ds_read_b64_tr_b16 v[168:169], v189 offset:0x820
	ds_read_b64_tr_b16 v[170:171], v189 offset:0xa20
	ds_read_b64_tr_b16 v[172:173], v189 offset:0xc20
	ds_read_b64_tr_b16 v[174:175], v189 offset:0xe20
	ds_read_b64_tr_b16 v[200:201], v189 offset:0x1040
	ds_read_b64_tr_b16 v[202:203], v189 offset:0x1240
	ds_read_b64_tr_b16 v[204:205], v189 offset:0x1440
	ds_read_b64_tr_b16 v[206:207], v189 offset:0x1640
	s_waitcnt lgkmcnt(4)
	s_nop 0
	v_mfma_f32_16x16x32_bf16 v[102:105], v[156:159], v[114:117], v[102:105]
	v_mfma_f32_16x16x32_bf16 v[98:101], v[156:159], v[118:121], v[98:101]
	v_mfma_f32_16x16x32_bf16 v[94:97], v[168:171], v[114:117], v[94:97]
	v_mfma_f32_16x16x32_bf16 v[90:93], v[168:171], v[118:121], v[90:93]
	v_mfma_f32_16x16x32_bf16 v[102:105], v[164:167], v[122:125], v[102:105]
	v_mfma_f32_16x16x32_bf16 v[98:101], v[164:167], v[126:129], v[98:101]
	v_mfma_f32_16x16x32_bf16 v[94:97], v[172:175], v[122:125], v[94:97]
	v_mfma_f32_16x16x32_bf16 v[90:93], v[172:175], v[126:129], v[90:93]
	ds_read_b64_tr_b16 v[156:157], v189 offset:0x1860
	ds_read_b64_tr_b16 v[158:159], v189 offset:0x1a60
	ds_read_b64_tr_b16 v[164:165], v189 offset:0x1c60
	ds_read_b64_tr_b16 v[166:167], v189 offset:0x1e60
	s_waitcnt lgkmcnt(4)
; #define SBAR() __builtin_amdgcn_sched_barrier(0)
; #define HLOADV(kt) do { const char* vb_ = (const char*)Vh + (size_t)(kt) * (64 * LDK * 2); sv0 = *(const bf16x8*)(vb_ + koff0); sv1 = *(const bf16x8*)(vb_ + koff1); } while (0)
; #define HLOADK(kt) do { const char* kb_ = (const char*)Kh + (size_t)(kt) * (64 * LDK * 2); sk0 = *(const bf16x8*)(kb_ + koff0); sk1 = *(const bf16x8*)(kb_ + koff1); } while (0)
; #define HWRITEV(b) do { char* d_ = V_lds + (b) * G16_V; *(bf16x8*)(d_ + vst0) = sv0; *(bf16x8*)(d_ + vst1) = sv1; } while (0)
; #define HWRITEK(b) do { char* d_ = K_lds + (b) * GB_K; *(bf16x8*)(d_ + KSWZ(sr, sc * 2)) = sk0; *(bf16x8*)(d_ + KSWZ(32 + sr, sc * 2)) = sk1; } while (0)
; #define HEXP() do { _Pragma("unroll") for (int kt = 0; kt < 4; ++kt) { _Pragma("unroll") for (int qt = 0; qt < 2; ++qt) { _Pragma("unroll") for (int i = 0; i < 4; ++i) s[kt][qt][i] = __builtin_amdgcn_exp2f(fmaf(s[kt][qt][i], C, mnC)); } } } while (0)
; template <int LDQ, int LDK, int LDO>
; __device__ __forceinline__ void attn_gqa16_body(const bf16* __restrict__ Qb, const bf16* __restrict__ Kh, const bf16* __restrict__ Vh, bf16* __restrict__ Ob, int seq, char* lds, float mref) {
;     ...
;     asm volatile("s_waitcnt vmcnt(0)" ::: "memory");
;     if (t + 2 < NT) HWRITEK(t & 1);
;     if (t + 1 < NT) HWRITEV((t + 1) & 1);
;     HLOADK(t + 3); HLOADV(t + 2);
;     SBAR(); pv16<4>(o, vb, pb); SBAR();
;     if (more) HEXP();
;   }
	v_mfma_f32_16x16x32_bf16 v[78:81], v[200:203], v[114:117], v[78:81]
	s_waitcnt lgkmcnt(0)
	v_mfma_f32_16x16x32_bf16 v[50:53], v[200:203], v[118:121], v[50:53]
	v_mfma_f32_16x16x32_bf16 v[78:81], v[204:207], v[122:125], v[78:81]
	v_mfma_f32_16x16x32_bf16 v[50:53], v[204:207], v[126:129], v[50:53]
	v_mfma_f32_16x16x32_bf16 v[82:85], v[156:159], v[114:117], v[82:85]
	v_mfma_f32_16x16x32_bf16 v[86:89], v[156:159], v[118:121], v[86:89]
	v_mfma_f32_16x16x32_bf16 v[82:85], v[164:167], v[122:125], v[82:85]
	v_mfma_f32_16x16x32_bf16 v[86:89], v[164:167], v[126:129], v[86:89]
	v_lshl_add_u64 v[152:153], v[162:163], 0, s[14:15]
	v_add_co_u32_e32 v156, vcc, s37, v152
	s_mulk_i32 s16, 0x4400
	s_nop 0
	v_addc_co_u32_e32 v157, vcc, 0, v153, vcc
	v_add_co_u32_e32 v158, vcc, s38, v152
	v_add_u32_e32 v164, s16, v194
	s_nop 0
	v_addc_co_u32_e32 v159, vcc, 0, v153, vcc
	s_waitcnt vmcnt(2)
	ds_write_b128 v164, v[106:109] offset:33280
	ds_write_b128 v164, v[110:113] offset:41984
	global_load_dwordx4 v[106:109], v[156:157], off offset:3072
	global_load_dwordx4 v[110:113], v[158:159], off offset:3072
	ds_read_b64_tr_b16 v[156:157], v189 offset:0x2080
	ds_read_b64_tr_b16 v[158:159], v189 offset:0x2280
	ds_read_b64_tr_b16 v[164:165], v189 offset:0x2480
	ds_read_b64_tr_b16 v[166:167], v189 offset:0x2680
	ds_read_b64_tr_b16 v[168:169], v189 offset:0x28a0
	ds_read_b64_tr_b16 v[170:171], v189 offset:0x2aa0
	ds_read_b64_tr_b16 v[172:173], v189 offset:0x2ca0
	ds_read_b64_tr_b16 v[174:175], v189 offset:0x2ea0
	ds_read_b64_tr_b16 v[200:201], v189 offset:0x30c0
	ds_read_b64_tr_b16 v[202:203], v189 offset:0x32c0
	ds_read_b64_tr_b16 v[204:205], v189 offset:0x34c0
	ds_read_b64_tr_b16 v[206:207], v189 offset:0x36c0
	s_waitcnt lgkmcnt(4)
	s_nop 0
	v_mfma_f32_16x16x32_bf16 v[54:57], v[156:159], v[114:117], v[54:57]
	v_mfma_f32_16x16x32_bf16 v[62:65], v[156:159], v[118:121], v[62:65]
	v_mfma_f32_16x16x32_bf16 v[58:61], v[168:171], v[114:117], v[58:61]
	v_mfma_f32_16x16x32_bf16 v[70:73], v[168:171], v[118:121], v[70:73]
	v_mfma_f32_16x16x32_bf16 v[54:57], v[164:167], v[122:125], v[54:57]
	v_mfma_f32_16x16x32_bf16 v[62:65], v[164:167], v[126:129], v[62:65]
	v_mfma_f32_16x16x32_bf16 v[58:61], v[172:175], v[122:125], v[58:61]
	v_mfma_f32_16x16x32_bf16 v[70:73], v[172:175], v[126:129], v[70:73]
	ds_read_b64_tr_b16 v[156:157], v189 offset:0x38e0
	ds_read_b64_tr_b16 v[158:159], v189 offset:0x3ae0
	ds_read_b64_tr_b16 v[164:165], v189 offset:0x3ce0
	ds_read_b64_tr_b16 v[166:167], v189 offset:0x3ee0
	s_waitcnt lgkmcnt(4)
	v_mfma_f32_16x16x32_bf16 v[42:45], v[200:203], v[114:117], v[42:45]
	s_waitcnt lgkmcnt(0)
	v_mfma_f32_16x16x32_bf16 v[46:49], v[200:203], v[118:121], v[46:49]
	v_mfma_f32_16x16x32_bf16 v[42:45], v[204:207], v[122:125], v[42:45]
	v_mfma_f32_16x16x32_bf16 v[46:49], v[204:207], v[126:129], v[46:49]
	v_mfma_f32_16x16x32_bf16 v[66:69], v[156:159], v[114:117], v[66:69]
	v_mfma_f32_16x16x32_bf16 v[74:77], v[156:159], v[118:121], v[74:77]
	v_mfma_f32_16x16x32_bf16 v[66:69], v[164:167], v[122:125], v[66:69]
	v_mfma_f32_16x16x32_bf16 v[74:77], v[164:167], v[126:129], v[74:77]
	v_fmamk_f32 v114, v196, 0x3e0293ee, v186
	v_exp_f32_e32 v158, v114
	v_fmamk_f32 v114, v197, 0x3e0293ee, v186
	v_exp_f32_e32 v152, v114
	v_fmamk_f32 v114, v198, 0x3e0293ee, v186
	v_exp_f32_e32 v156, v114
	v_fmamk_f32 v114, v199, 0x3e0293ee, v186
	v_exp_f32_e32 v160, v114
	v_fmamk_f32 v114, v220, 0x3e0293ee, v186
	v_exp_f32_e32 v159, v114
	v_fmamk_f32 v114, v221, 0x3e0293ee, v186
	v_exp_f32_e32 v153, v114
	v_fmamk_f32 v114, v222, 0x3e0293ee, v186
	v_exp_f32_e32 v157, v114
	v_fmamk_f32 v114, v223, 0x3e0293ee, v186
	v_exp_f32_e32 v161, v114
	v_fmamk_f32 v114, v224, 0x3e0293ee, v186
	v_exp_f32_e32 v168, v114
	v_fmamk_f32 v114, v225, 0x3e0293ee, v186
	v_exp_f32_e32 v170, v114
	v_fmamk_f32 v114, v226, 0x3e0293ee, v186
	v_exp_f32_e32 v164, v114
	v_fmamk_f32 v114, v227, 0x3e0293ee, v186
	v_exp_f32_e32 v166, v114
	v_fmamk_f32 v114, v146, 0x3e0293ee, v186
	v_exp_f32_e32 v169, v114
	v_fmamk_f32 v114, v147, 0x3e0293ee, v186
	v_exp_f32_e32 v171, v114
	v_fmamk_f32 v114, v148, 0x3e0293ee, v186
	v_exp_f32_e32 v165, v114
	v_fmamk_f32 v114, v149, 0x3e0293ee, v186
	v_exp_f32_e32 v167, v114
	v_fmamk_f32 v114, v142, 0x3e0293ee, v186
	v_exp_f32_e32 v142, v114
	v_fmamk_f32 v114, v143, 0x3e0293ee, v186
	v_exp_f32_e32 v172, v114
	v_fmamk_f32 v114, v144, 0x3e0293ee, v186
	v_exp_f32_e32 v144, v114
	v_fmamk_f32 v114, v145, 0x3e0293ee, v186
	v_exp_f32_e32 v174, v114
	v_fmamk_f32 v114, v138, 0x3e0293ee, v186
	v_exp_f32_e32 v143, v114
	v_fmamk_f32 v114, v139, 0x3e0293ee, v186
	v_exp_f32_e32 v173, v114
	v_fmamk_f32 v114, v140, 0x3e0293ee, v186
	v_exp_f32_e32 v145, v114
	v_fmamk_f32 v114, v141, 0x3e0293ee, v186
	v_exp_f32_e32 v175, v114
	v_fmamk_f32 v114, v134, 0x3e0293ee, v186
	v_exp_f32_e32 v134, v114
	v_fmamk_f32 v114, v135, 0x3e0293ee, v186
	v_exp_f32_e32 v138, v114
	v_fmamk_f32 v114, v136, 0x3e0293ee, v186
	v_exp_f32_e32 v136, v114
	v_fmamk_f32 v114, v137, 0x3e0293ee, v186
	v_exp_f32_e32 v140, v114
	v_fmamk_f32 v114, v130, 0x3e0293ee, v186
	v_exp_f32_e32 v135, v114
	v_fmamk_f32 v114, v131, 0x3e0293ee, v186
	v_exp_f32_e32 v139, v114
	v_fmamk_f32 v114, v132, 0x3e0293ee, v186
	v_exp_f32_e32 v137, v114
	v_fmamk_f32 v114, v133, 0x3e0293ee, v186
	v_exp_f32_e32 v141, v114
	s_add_u32 s14, s14, 0x90000
	s_addc_u32 s15, s15, 0
	s_cmp_lg_u32 s14, 0x9120000
	s_mov_b32 s16, s17
	s_cbranch_scc1 .LBB0_650
; #define SBAR() __builtin_amdgcn_sched_barrier(0)
; template <int LDQ, int LDK, int LDO>
; __device__ __forceinline__ void attn_gqa16_body(const bf16* __restrict__ Qb, const bf16* __restrict__ Kh, const bf16* __restrict__ Vh, bf16* __restrict__ Ob, int seq, char* lds, float mref) {
;     ...
;   for (int t = 0; t < NT; ++t) {
;     HPACK();
;     __syncthreads();
;     const bool more = t + 1 < NT;
;     if (more) HQK((t + 1) & 1);
;     const int vb = vb0 + (t & 1) * (int)G16_V;
;     SBAR(); pv16<0>(o, vb, pb); SBAR();
	s_waitcnt vmcnt(1)
	v_cvt_pk_bf16_f32 v106, v158, v152
	v_cvt_pk_bf16_f32 v107, v156, v160
	v_cvt_pk_bf16_f32 v108, v168, v170
	v_cvt_pk_bf16_f32 v109, v164, v166
	s_waitcnt vmcnt(0)
	v_cvt_pk_bf16_f32 v110, v159, v153
	v_cvt_pk_bf16_f32 v111, v157, v161
	v_cvt_pk_bf16_f32 v112, v169, v171
	v_cvt_pk_bf16_f32 v113, v165, v167
	v_cvt_pk_bf16_f32 v114, v142, v172
	v_cvt_pk_bf16_f32 v115, v144, v174
	v_cvt_pk_bf16_f32 v116, v134, v138
	v_cvt_pk_bf16_f32 v117, v136, v140
	v_cvt_pk_bf16_f32 v118, v143, v173
	v_cvt_pk_bf16_f32 v119, v145, v175
	v_cvt_pk_bf16_f32 v120, v135, v139
	v_cvt_pk_bf16_f32 v121, v137, v141
	s_waitcnt lgkmcnt(0)
	s_barrier
	s_mov_b32 m0, s86
	s_nop 0
	global_load_lds_dwordx4 v253, s[74:75]
	s_add_i32 m0, s86, 0x400
	s_nop 0
	global_load_lds_dwordx4 v253, s[76:77]
	ds_read_b128 v[122:125], v182 offset:50688
	ds_read_b128 v[126:129], v182 offset:50752
	ds_read_b128 v[146:149], v182 offset:55040
	ds_read_b128 v[196:199], v182 offset:55104
	ds_read_b128 v[204:207], v182 offset:59392
	ds_read_b128 v[208:211], v182 offset:59456
	ds_read_b128 v[216:219], v182 offset:63744
	ds_read_b128 v[220:223], v182 offset:63808
	s_waitcnt lgkmcnt(7)
	v_mfma_f32_16x16x32_bf16 v[130:133], v[122:125], v[30:33], 0
	v_mov_b32_e32 v190, v168
	v_mov_b32_e32 v191, v158
	v_mov_b32_e32 v192, v170
	v_mfma_f32_16x16x32_bf16 v[122:125], v[122:125], v[38:41], 0
	v_mov_b32_e32 v193, v152
	v_mov_b32_e32 v152, v171
	s_lshl_b32 s8, s8, 12
	s_waitcnt lgkmcnt(5)
	v_mfma_f32_16x16x32_bf16 v[200:203], v[146:149], v[30:33], 0
	s_add_u32 s8, s42, s8
	s_addc_u32 s14, s43, 0
	s_add_u32 s12, s8, s12
	v_mfma_f32_16x16x32_bf16 v[146:149], v[146:149], v[38:41], 0
	s_addc_u32 s13, s14, s13
	s_waitcnt lgkmcnt(3)
	v_mfma_f32_16x16x32_bf16 v[212:215], v[204:207], v[30:33], 0
	s_waitcnt lgkmcnt(1)
	v_mfma_f32_16x16x32_bf16 v[30:33], v[216:219], v[30:33], 0
	v_mfma_f32_16x16x32_bf16 v[130:133], v[126:129], v[18:21], v[130:133]
	v_mfma_f32_16x16x32_bf16 v[122:125], v[126:129], v[22:25], v[122:125]
	v_mfma_f32_16x16x32_bf16 v[126:129], v[196:199], v[18:21], v[200:203]
	v_mfma_f32_16x16x32_bf16 v[146:149], v[196:199], v[22:25], v[146:149]
	v_mfma_f32_16x16x32_bf16 v[196:199], v[208:211], v[18:21], v[212:215]
	s_waitcnt lgkmcnt(0)
	v_mfma_f32_16x16x32_bf16 v[18:21], v[220:223], v[18:21], v[30:33]
	s_nop 0
	v_mov_b32_e32 v213, v156
	v_mov_b32_e32 v212, v164
	v_mov_b32_e32 v214, v166
	ds_read_b128 v[30:33], v182 offset:50816
	v_mfma_f32_16x16x32_bf16 v[204:207], v[204:207], v[38:41], 0
	v_mov_b32_e32 v215, v160
	v_mfma_f32_16x16x32_bf16 v[38:41], v[216:219], v[38:41], 0
	v_mov_b32_e32 v216, v169
	v_mov_b32_e32 v217, v159
	v_mov_b32_e32 v219, v157
	v_mfma_f32_16x16x32_bf16 v[200:203], v[208:211], v[22:25], v[204:207]
	v_mov_b32_e32 v218, v165
	v_mfma_f32_16x16x32_bf16 v[22:25], v[220:223], v[22:25], v[38:41]
	s_nop 2
	ds_read_b128 v[38:41], v182 offset:55168
	ds_read_b128 v[204:207], v182 offset:50880
	s_waitcnt lgkmcnt(2)
	v_mfma_f32_16x16x32_bf16 v[130:133], v[30:33], v[10:13], v[130:133]
	v_mfma_f32_16x16x32_bf16 v[30:33], v[30:33], v[14:17], v[122:125]
	s_nop 2
	ds_read_b128 v[122:125], v182 offset:59520
	ds_read_b128 v[208:211], v182 offset:55232
	s_waitcnt lgkmcnt(3)
	v_mfma_f32_16x16x32_bf16 v[126:129], v[38:41], v[10:13], v[126:129]
	v_mfma_f32_16x16x32_bf16 v[38:41], v[38:41], v[14:17], v[146:149]
	s_nop 2
	ds_read_b128 v[146:149], v182 offset:63872
	ds_read_b128 v[168:171], v182 offset:59584
	ds_read_b128 v[156:159], v182 offset:63936
	s_waitcnt lgkmcnt(4)
	v_mfma_f32_16x16x32_bf16 v[196:199], v[122:125], v[10:13], v[196:199]
	s_waitcnt lgkmcnt(2)
	v_mfma_f32_16x16x32_bf16 v[10:13], v[146:149], v[10:13], v[18:21]
	v_mfma_f32_16x16x32_bf16 v[122:125], v[122:125], v[14:17], v[200:203]
	s_nop 1
	v_mov_b32_e32 v18, v142
	v_mov_b32_e32 v19, v144
	v_mov_b32_e32 v20, v172
	v_mfma_f32_16x16x32_bf16 v[14:17], v[146:149], v[14:17], v[22:25]
	v_mov_b32_e32 v201, v161
	v_mov_b32_e32 v200, v167
	v_mov_b32_e32 v21, v174
	v_mfma_f32_16x16x32_bf16 v[160:163], v[204:207], v[6:9], v[30:33]
	v_add_f32_e64 v24, v190, v192
	v_add_f32_e64 v25, v191, v193
	v_mov_b32_e32 v144, v143
	v_mov_b32_e32 v22, v173
	v_pk_add_f32 v[30:31], v[212:213], v[214:215]
	v_mfma_f32_16x16x32_bf16 v[146:149], v[204:207], v[2:5], v[130:133]
	v_add_f32_e64 v24, v24, v30
	v_add_f32_e64 v25, v25, v31
	v_mov_b32_e32 v23, v175
	v_pk_add_f32 v[32:33], v[216:217], v[152:153]
	v_mfma_f32_16x16x32_bf16 v[164:167], v[208:211], v[2:5], v[126:129]
	v_add_f32_e64 v144, v144, v22
	v_add_f32_e64 v145, v145, v23
	v_add_f32_e32 v130, v134, v138
	v_add_f32_e32 v132, v136, v140
	v_mfma_f32_16x16x32_bf16 v[172:175], v[208:211], v[6:9], v[38:41]
	v_add_f32_e64 v126, v18, v20
	v_add_f32_e64 v127, v19, v21
	s_nop 0
	v_pk_add_f32 v[38:39], v[218:219], v[200:201]
	s_waitcnt lgkmcnt(1)
	v_mfma_f32_16x16x32_bf16 v[196:199], v[168:171], v[2:5], v[196:199]
	v_add_f32_e64 v142, v32, v38
	v_add_f32_e64 v143, v33, v39
	s_waitcnt lgkmcnt(0)
	v_mfma_f32_16x16x32_bf16 v[200:203], v[156:159], v[2:5], v[10:13]
	v_add_f32_e64 v2, v150, v25
	v_add_f32_e64 v3, v151, v24
	v_pk_add_f32 v[128:129], v[24:25], v[2:3]
	v_mfma_f32_16x16x32_bf16 v[168:171], v[168:171], v[6:9], v[122:125]
	s_nop 2
	v_add_f32_e32 v122, v135, v139
	v_add_f32_e32 v124, v137, v141
	v_mfma_f32_16x16x32_bf16 v[134:137], v[156:159], v[6:9], v[14:17]
	ds_read_b64_tr_b16 v[2:3], v183 offset:0
	ds_read_b64_tr_b16 v[4:5], v183 offset:0x200
	ds_read_b64_tr_b16 v[6:7], v183 offset:0x400
	ds_read_b64_tr_b16 v[8:9], v183 offset:0x600
	ds_read_b64_tr_b16 v[10:11], v183 offset:0x820
	ds_read_b64_tr_b16 v[12:13], v183 offset:0xa20
	ds_read_b64_tr_b16 v[14:15], v183 offset:0xc20
	ds_read_b64_tr_b16 v[16:17], v183 offset:0xe20
	ds_read_b64_tr_b16 v[18:19], v183 offset:0x1040
	ds_read_b64_tr_b16 v[20:21], v183 offset:0x1240
	ds_read_b64_tr_b16 v[22:23], v183 offset:0x1440
	ds_read_b64_tr_b16 v[24:25], v183 offset:0x1640
	s_waitcnt lgkmcnt(4)
; #define SBAR() __builtin_amdgcn_sched_barrier(0)
; #define HLOADV(kt) do { const char* vb_ = (const char*)Vh + (size_t)(kt) * (64 * LDK * 2); sv0 = *(const bf16x8*)(vb_ + koff0); sv1 = *(const bf16x8*)(vb_ + koff1); } while (0)
; #define HLOADK(kt) do { const char* kb_ = (const char*)Kh + (size_t)(kt) * (64 * LDK * 2); sk0 = *(const bf16x8*)(kb_ + koff0); sk1 = *(const bf16x8*)(kb_ + koff1); } while (0)
; #define HWRITEV(b) do { char* d_ = V_lds + (b) * G16_V; *(bf16x8*)(d_ + vst0) = sv0; *(bf16x8*)(d_ + vst1) = sv1; } while (0)
; #define HWRITEK(b) do { char* d_ = K_lds + (b) * GB_K; *(bf16x8*)(d_ + KSWZ(sr, sc * 2)) = sk0; *(bf16x8*)(d_ + KSWZ(32 + sr, sc * 2)) = sk1; } while (0)
; #define HEXP() do { _Pragma("unroll") for (int kt = 0; kt < 4; ++kt) { _Pragma("unroll") for (int qt = 0; qt < 2; ++qt) { _Pragma("unroll") for (int i = 0; i < 4; ++i) s[kt][qt][i] = __builtin_amdgcn_exp2f(fmaf(s[kt][qt][i], C, mnC)); } } } while (0)
; template <int LDQ, int LDK, int LDO>
; __device__ __forceinline__ void attn_gqa16_body(const bf16* __restrict__ Qb, const bf16* __restrict__ Kh, const bf16* __restrict__ Vh, bf16* __restrict__ Ob, int seq, char* lds, float mref) {
;     ...
;   for (int t = 0; t < NT; ++t) {
;     HPACK();
;     __syncthreads();
;     const bool more = t + 1 < NT;
;     if (more) HQK((t + 1) & 1);
;     const int vb = vb0 + (t & 1) * (int)G16_V;
;     SBAR(); pv16<0>(o, vb, pb); SBAR();
;     asm volatile("s_waitcnt vmcnt(0)" ::: "memory");
;     if (t + 2 < NT) HWRITEK(t & 1);
;     if (t + 1 < NT) HWRITEV((t + 1) & 1);
;     HLOADK(t + 3); HLOADV(t + 2);
;     SBAR(); pv16<4>(o, vb, pb); SBAR();
;     if (more) HEXP();
;   }
	s_nop 0
	v_mfma_f32_16x16x32_bf16 v[30:33], v[2:5], v[106:109], v[102:105]
	v_mfma_f32_16x16x32_bf16 v[38:41], v[2:5], v[110:113], v[98:101]
	v_mfma_f32_16x16x32_bf16 v[94:97], v[10:13], v[106:109], v[94:97]
	v_mfma_f32_16x16x32_bf16 v[10:13], v[10:13], v[110:113], v[90:93]
	v_mfma_f32_16x16x32_bf16 v[2:5], v[6:9], v[114:117], v[30:33]
	v_mfma_f32_16x16x32_bf16 v[6:9], v[6:9], v[118:121], v[38:41]
	v_mfma_f32_16x16x32_bf16 v[38:41], v[14:17], v[114:117], v[94:97]
	v_mfma_f32_16x16x32_bf16 v[90:93], v[14:17], v[118:121], v[10:13]
	ds_read_b64_tr_b16 v[14:15], v183 offset:0x1860
	ds_read_b64_tr_b16 v[16:17], v183 offset:0x1a60
	ds_read_b64_tr_b16 v[30:31], v183 offset:0x1c60
	ds_read_b64_tr_b16 v[32:33], v183 offset:0x1e60
	s_waitcnt lgkmcnt(4)
	v_mfma_f32_16x16x32_bf16 v[10:13], v[18:21], v[106:109], v[78:81]
	s_waitcnt lgkmcnt(0)
	v_mfma_f32_16x16x32_bf16 v[18:21], v[18:21], v[110:113], v[50:53]
	v_mfma_f32_16x16x32_bf16 v[10:13], v[22:25], v[114:117], v[10:13]
	v_mfma_f32_16x16x32_bf16 v[22:25], v[22:25], v[118:121], v[18:21]
	v_mfma_f32_16x16x32_bf16 v[18:21], v[14:17], v[106:109], v[82:85]
	v_mfma_f32_16x16x32_bf16 v[50:53], v[14:17], v[110:113], v[86:89]
	v_mfma_f32_16x16x32_bf16 v[14:17], v[30:33], v[114:117], v[18:21]
	v_mfma_f32_16x16x32_bf16 v[18:21], v[30:33], v[118:121], v[50:53]
	s_waitcnt vmcnt(0)
	s_waitcnt vmcnt(1)
	s_waitcnt vmcnt(0)
	ds_read_b64_tr_b16 v[26:27], v183 offset:0x2080
	ds_read_b64_tr_b16 v[28:29], v183 offset:0x2280
	ds_read_b64_tr_b16 v[30:31], v183 offset:0x2480
	ds_read_b64_tr_b16 v[32:33], v183 offset:0x2680
	ds_read_b64_tr_b16 v[34:35], v183 offset:0x28a0
	ds_read_b64_tr_b16 v[36:37], v183 offset:0x2aa0
	ds_read_b64_tr_b16 v[78:79], v183 offset:0x2ca0
	ds_read_b64_tr_b16 v[80:81], v183 offset:0x2ea0
	ds_read_b64_tr_b16 v[82:83], v183 offset:0x30c0
	ds_read_b64_tr_b16 v[84:85], v183 offset:0x32c0
	ds_read_b64_tr_b16 v[86:87], v183 offset:0x34c0
	ds_read_b64_tr_b16 v[88:89], v183 offset:0x36c0
	s_waitcnt lgkmcnt(4)
	s_nop 0
	v_mfma_f32_16x16x32_bf16 v[50:53], v[26:29], v[106:109], v[54:57]
	v_mfma_f32_16x16x32_bf16 v[26:29], v[26:29], v[110:113], v[62:65]
	v_mfma_f32_16x16x32_bf16 v[58:61], v[34:37], v[106:109], v[58:61]
	v_mfma_f32_16x16x32_bf16 v[34:37], v[34:37], v[110:113], v[70:73]
	v_mfma_f32_16x16x32_bf16 v[50:53], v[30:33], v[114:117], v[50:53]
	v_mfma_f32_16x16x32_bf16 v[54:57], v[30:33], v[118:121], v[26:29]
	v_mfma_f32_16x16x32_bf16 v[70:73], v[78:81], v[114:117], v[58:61]
	v_mfma_f32_16x16x32_bf16 v[78:81], v[78:81], v[118:121], v[34:37]
	ds_read_b64_tr_b16 v[30:31], v183 offset:0x38e0
	ds_read_b64_tr_b16 v[32:33], v183 offset:0x3ae0
	ds_read_b64_tr_b16 v[34:35], v183 offset:0x3ce0
	ds_read_b64_tr_b16 v[36:37], v183 offset:0x3ee0
	s_waitcnt lgkmcnt(4)
	v_mfma_f32_16x16x32_bf16 v[26:29], v[82:85], v[106:109], v[42:45]
	s_waitcnt lgkmcnt(0)
	v_mfma_f32_16x16x32_bf16 v[42:45], v[82:85], v[110:113], v[46:49]
	v_mfma_f32_16x16x32_bf16 v[26:29], v[86:89], v[114:117], v[26:29]
	v_mfma_f32_16x16x32_bf16 v[58:61], v[86:89], v[118:121], v[42:45]
	v_mfma_f32_16x16x32_bf16 v[42:45], v[30:33], v[106:109], v[66:69]
	v_mfma_f32_16x16x32_bf16 v[46:49], v[30:33], v[110:113], v[74:77]
	v_mfma_f32_16x16x32_bf16 v[30:33], v[34:37], v[114:117], v[42:45]
	v_mfma_f32_16x16x32_bf16 v[62:65], v[34:37], v[118:121], v[46:49]
	s_nop 4
	v_fmamk_f32 v42, v196, 0x3e0293ee, v186
	v_exp_f32_e32 v116, v42
	v_fmamk_f32 v42, v197, 0x3e0293ee, v186
	v_exp_f32_e32 v117, v42
	v_fmamk_f32 v42, v198, 0x3e0293ee, v186
	v_exp_f32_e32 v118, v42
	v_fmamk_f32 v42, v199, 0x3e0293ee, v186
	v_exp_f32_e32 v119, v42
	v_fmamk_f32 v42, v168, 0x3e0293ee, v186
	v_fmamk_f32 v34, v146, 0x3e0293ee, v186
	v_exp_f32_e32 v98, v42
	v_fmamk_f32 v42, v169, 0x3e0293ee, v186
	v_exp_f32_e32 v131, v34
	v_fmamk_f32 v34, v147, 0x3e0293ee, v186
	v_exp_f32_e32 v99, v42
	v_fmamk_f32 v42, v170, 0x3e0293ee, v186
	v_exp_f32_e32 v133, v34
	v_fmamk_f32 v34, v148, 0x3e0293ee, v186
	v_exp_f32_e32 v100, v42
	v_fmamk_f32 v42, v171, 0x3e0293ee, v186
	v_exp_f32_e32 v74, v34
	v_fmamk_f32 v34, v149, 0x3e0293ee, v186
	v_exp_f32_e32 v101, v42
	v_fmamk_f32 v42, v200, 0x3e0293ee, v186
	v_exp_f32_e32 v129, v34
	v_fmamk_f32 v34, v160, 0x3e0293ee, v186
	v_exp_f32_e32 v120, v42
	v_fmamk_f32 v42, v201, 0x3e0293ee, v186
	v_exp_f32_e32 v123, v34
	v_fmamk_f32 v34, v161, 0x3e0293ee, v186
	v_exp_f32_e32 v121, v42
	v_fmamk_f32 v42, v202, 0x3e0293ee, v186
	v_exp_f32_e32 v125, v34
	v_fmamk_f32 v34, v162, 0x3e0293ee, v186
	v_exp_f32_e32 v75, v42
	v_fmamk_f32 v42, v203, 0x3e0293ee, v186
	v_exp_f32_e32 v76, v34
	v_fmamk_f32 v34, v163, 0x3e0293ee, v186
	v_exp_f32_e32 v77, v42
	v_fmamk_f32 v42, v134, 0x3e0293ee, v186
	v_exp_f32_e32 v87, v34
	v_fmamk_f32 v34, v164, 0x3e0293ee, v186
	v_exp_f32_e32 v102, v42
	v_fmamk_f32 v42, v135, 0x3e0293ee, v186
	v_exp_f32_e32 v66, v34
	v_fmamk_f32 v34, v165, 0x3e0293ee, v186
	v_exp_f32_e32 v103, v42
	v_fmamk_f32 v42, v136, 0x3e0293ee, v186
	v_exp_f32_e32 v68, v34
	v_fmamk_f32 v34, v166, 0x3e0293ee, v186
	v_exp_f32_e32 v43, v42
	v_exp_f32_e32 v67, v34
	v_fmamk_f32 v34, v167, 0x3e0293ee, v186
	v_fmamk_f32 v35, v173, 0x3e0293ee, v186
	v_exp_f32_e32 v69, v34
	v_fmamk_f32 v34, v172, 0x3e0293ee, v186
	v_exp_f32_e32 v36, v35
	v_fmamk_f32 v35, v174, 0x3e0293ee, v186
	v_fmamk_f32 v37, v175, 0x3e0293ee, v186
	v_fmamk_f32 v42, v137, 0x3e0293ee, v186
	v_exp_f32_e32 v34, v34
	v_exp_f32_e32 v35, v35
	v_exp_f32_e32 v37, v37
	v_exp_f32_e32 v45, v42
	v_add_f32_e32 v42, v143, v151
	v_pk_add_f32 v[48:49], v[144:145], v[144:145] op_sel:[0,1] op_sel_hi:[1,0]
	v_pk_add_f32 v[84:85], v[142:143], v[42:43] op_sel_hi:[1,0]
	v_mov_b32_e32 v49, v76
	v_mov_b32_e32 v85, v87
	v_pk_add_f32 v[46:47], v[122:123], v[124:125]
	v_pk_add_f32 v[48:49], v[48:49], v[84:85]
	v_add_f32_e32 v42, v98, v99
	v_pk_add_f32 v[46:47], v[46:47], v[48:49]
	v_pk_add_f32 v[48:49], v[34:35], v[36:37]
	v_pk_add_f32 v[46:47], v[46:47], v[46:47] op_sel:[0,1] op_sel_hi:[1,0]
	v_pk_add_f32 v[48:49], v[48:49], v[48:49] op_sel:[0,1] op_sel_hi:[1,0]
	v_add_f32_e32 v44, v100, v101
	v_mov_b32_e32 v47, v102
	v_mov_b32_e32 v49, v103
	v_pk_add_f32 v[46:47], v[46:47], v[48:49]
	v_pk_add_f32 v[48:49], v[42:43], v[44:45]
	v_cvt_pk_bf16_f32 v82, v131, v133
	v_cvt_pk_bf16_f32 v83, v74, v129
	v_cvt_pk_bf16_f32 v84, v66, v68
	v_cvt_pk_bf16_f32 v85, v67, v69
	v_cvt_pk_bf16_f32 v86, v123, v125
	s_nop 0
	v_pk_add_f32 v[46:47], v[46:47], v[48:49]
	v_pk_add_f32 v[48:49], v[126:127], v[126:127] op_sel:[0,1] op_sel_hi:[1,0]
	v_add_f32_e32 v122, v46, v47
	v_mov_b32_e32 v49, v74
	v_pk_add_f32 v[46:47], v[130:131], v[132:133]
	v_pk_add_f32 v[48:49], v[48:49], v[128:129]
	v_cvt_pk_bf16_f32 v87, v76, v87
	v_cvt_pk_bf16_f32 v88, v34, v36
	v_cvt_pk_bf16_f32 v89, v35, v37
	v_cvt_pk_bf16_f32 v94, v116, v117
	v_cvt_pk_bf16_f32 v95, v118, v119
	s_nop 0
	v_pk_add_f32 v[114:115], v[46:47], v[48:49]
	v_cvt_pk_bf16_f32 v96, v120, v121
	v_cvt_pk_bf16_f32 v97, v75, v77
	v_cvt_pk_bf16_f32 v98, v98, v99
	v_cvt_pk_bf16_f32 v99, v100, v101
	v_cvt_pk_bf16_f32 v100, v102, v103
	v_cvt_pk_bf16_f32 v101, v43, v45
	s_waitcnt lgkmcnt(0)
	s_barrier
; #define SBAR() __builtin_amdgcn_sched_barrier(0)
; #define HLOADV(kt) do { const char* vb_ = (const char*)Vh + (size_t)(kt) * (64 * LDK * 2); sv0 = *(const bf16x8*)(vb_ + koff0); sv1 = *(const bf16x8*)(vb_ + koff1); } while (0)
; #define HLOADK(kt) do { const char* kb_ = (const char*)Kh + (size_t)(kt) * (64 * LDK * 2); sk0 = *(const bf16x8*)(kb_ + koff0); sk1 = *(const bf16x8*)(kb_ + koff1); } while (0)
; #define HWRITEV(b) do { char* d_ = V_lds + (b) * G16_V; *(bf16x8*)(d_ + vst0) = sv0; *(bf16x8*)(d_ + vst1) = sv1; } while (0)
; #define HWRITEK(b) do { char* d_ = K_lds + (b) * GB_K; *(bf16x8*)(d_ + KSWZ(sr, sc * 2)) = sk0; *(bf16x8*)(d_ + KSWZ(32 + sr, sc * 2)) = sk1; } while (0)
; #define HEXP() do { _Pragma("unroll") for (int kt = 0; kt < 4; ++kt) { _Pragma("unroll") for (int qt = 0; qt < 2; ++qt) { _Pragma("unroll") for (int i = 0; i < 4; ++i) s[kt][qt][i] = __builtin_amdgcn_exp2f(fmaf(s[kt][qt][i], C, mnC)); } } } while (0)
; template <int LDQ, int LDK, int LDO>
; __device__ __forceinline__ void attn_gqa16_body(const bf16* __restrict__ Qb, const bf16* __restrict__ Kh, const bf16* __restrict__ Vh, bf16* __restrict__ Ob, int seq, char* lds, float mref) {
;     ...
;   for (int t = 0; t < NT; ++t) {
;     HPACK();
;     __syncthreads();
;     const bool more = t + 1 < NT;
;     if (more) HQK((t + 1) & 1);
;     const int vb = vb0 + (t & 1) * (int)G16_V;
;     SBAR(); pv16<0>(o, vb, pb); SBAR();
;     asm volatile("s_waitcnt vmcnt(0)" ::: "memory");
;     if (t + 2 < NT) HWRITEK(t & 1);
;     if (t + 1 < NT) HWRITEV((t + 1) & 1);
;     HLOADK(t + 3); HLOADV(t + 2);
;     SBAR(); pv16<4>(o, vb, pb); SBAR();
;     if (more) HEXP();
;   }
;   __builtin_amdgcn_s_setprio(0);
;   ls0 += __shfl_xor(ls0, 16); ls0 += __shfl_xor(ls0, 32); ls1 += __shfl_xor(ls1, 16); ls1 += __shfl_xor(ls1, 32);
;   const float rl[2] = {__builtin_amdgcn_rcpf(ls0), __builtin_amdgcn_rcpf(ls1)};
	ds_read_b64_tr_b16 v[34:35], v184 offset:0
	ds_read_b64_tr_b16 v[36:37], v184 offset:0x200
	ds_read_b64_tr_b16 v[42:43], v184 offset:0x400
	ds_read_b64_tr_b16 v[44:45], v184 offset:0x600
	ds_read_b64_tr_b16 v[46:47], v184 offset:0x820
	ds_read_b64_tr_b16 v[48:49], v184 offset:0xa20
	ds_read_b64_tr_b16 v[102:103], v184 offset:0xc20
	ds_read_b64_tr_b16 v[104:105], v184 offset:0xe20
	ds_read_b64_tr_b16 v[106:107], v184 offset:0x1040
	ds_read_b64_tr_b16 v[108:109], v184 offset:0x1240
	ds_read_b64_tr_b16 v[110:111], v184 offset:0x1440
	ds_read_b64_tr_b16 v[112:113], v184 offset:0x1640
	s_waitcnt lgkmcnt(4)
	s_nop 0
	v_mfma_f32_16x16x32_bf16 v[2:5], v[34:37], v[82:85], v[2:5]
	v_mfma_f32_16x16x32_bf16 v[6:9], v[34:37], v[86:89], v[6:9]
	v_mfma_f32_16x16x32_bf16 v[34:37], v[46:49], v[82:85], v[38:41]
	v_mfma_f32_16x16x32_bf16 v[46:49], v[46:49], v[86:89], v[90:93]
	v_mfma_f32_16x16x32_bf16 v[38:41], v[42:45], v[94:97], v[2:5]
	v_mfma_f32_16x16x32_bf16 v[6:9], v[42:45], v[98:101], v[6:9]
	v_mfma_f32_16x16x32_bf16 v[34:37], v[102:105], v[94:97], v[34:37]
	v_mfma_f32_16x16x32_bf16 v[2:5], v[102:105], v[98:101], v[46:49]
	ds_read_b64_tr_b16 v[46:47], v184 offset:0x1860
	ds_read_b64_tr_b16 v[48:49], v184 offset:0x1a60
	ds_read_b64_tr_b16 v[90:91], v184 offset:0x1c60
	ds_read_b64_tr_b16 v[92:93], v184 offset:0x1e60
	s_waitcnt lgkmcnt(4)
	v_mfma_f32_16x16x32_bf16 v[10:13], v[106:109], v[82:85], v[10:13]
	s_waitcnt lgkmcnt(0)
	v_mfma_f32_16x16x32_bf16 v[22:25], v[106:109], v[86:89], v[22:25]
	v_mfma_f32_16x16x32_bf16 v[42:45], v[110:113], v[94:97], v[10:13]
	v_mfma_f32_16x16x32_bf16 v[10:13], v[110:113], v[98:101], v[22:25]
	v_mfma_f32_16x16x32_bf16 v[14:17], v[46:49], v[82:85], v[14:17]
	v_mfma_f32_16x16x32_bf16 v[18:21], v[46:49], v[86:89], v[18:21]
	v_mfma_f32_16x16x32_bf16 v[46:49], v[90:93], v[94:97], v[14:17]
	v_mfma_f32_16x16x32_bf16 v[14:17], v[90:93], v[98:101], v[18:21]
	s_waitcnt vmcnt(0)
	ds_read_b64_tr_b16 v[18:19], v184 offset:0x2080
	ds_read_b64_tr_b16 v[20:21], v184 offset:0x2280
	ds_read_b64_tr_b16 v[22:23], v184 offset:0x2480
	ds_read_b64_tr_b16 v[24:25], v184 offset:0x2680
	ds_read_b64_tr_b16 v[90:91], v184 offset:0x28a0
	ds_read_b64_tr_b16 v[92:93], v184 offset:0x2aa0
	ds_read_b64_tr_b16 v[102:103], v184 offset:0x2ca0
	ds_read_b64_tr_b16 v[104:105], v184 offset:0x2ea0
	ds_read_b64_tr_b16 v[106:107], v184 offset:0x30c0
	ds_read_b64_tr_b16 v[108:109], v184 offset:0x32c0
	ds_read_b64_tr_b16 v[110:111], v184 offset:0x34c0
	ds_read_b64_tr_b16 v[112:113], v184 offset:0x36c0
	s_waitcnt lgkmcnt(4)
	s_nop 5
	v_mfma_f32_16x16x32_bf16 v[50:53], v[18:21], v[82:85], v[50:53]
	v_mfma_f32_16x16x32_bf16 v[18:21], v[18:21], v[86:89], v[54:57]
	v_mfma_f32_16x16x32_bf16 v[70:73], v[90:93], v[82:85], v[70:73]
	v_mfma_f32_16x16x32_bf16 v[78:81], v[90:93], v[86:89], v[78:81]
	v_mfma_f32_16x16x32_bf16 v[54:57], v[22:25], v[94:97], v[50:53]
	v_mfma_f32_16x16x32_bf16 v[22:25], v[22:25], v[98:101], v[18:21]
	v_mfma_f32_16x16x32_bf16 v[50:53], v[102:105], v[94:97], v[70:73]
	v_mfma_f32_16x16x32_bf16 v[18:21], v[102:105], v[98:101], v[78:81]
	ds_read_b64_tr_b16 v[70:71], v184 offset:0x38e0
	ds_read_b64_tr_b16 v[72:73], v184 offset:0x3ae0
	ds_read_b64_tr_b16 v[78:79], v184 offset:0x3ce0
	ds_read_b64_tr_b16 v[80:81], v184 offset:0x3ee0
	s_waitcnt lgkmcnt(4)
	v_mfma_f32_16x16x32_bf16 v[26:29], v[106:109], v[82:85], v[26:29]
	s_waitcnt lgkmcnt(0)
	v_mfma_f32_16x16x32_bf16 v[90:93], v[106:109], v[86:89], v[58:61]
	v_mfma_f32_16x16x32_bf16 v[58:61], v[110:113], v[94:97], v[26:29]
	v_mfma_f32_16x16x32_bf16 v[26:29], v[110:113], v[98:101], v[90:93]
	v_mfma_f32_16x16x32_bf16 v[30:33], v[70:73], v[82:85], v[30:33]
	v_mfma_f32_16x16x32_bf16 v[70:73], v[70:73], v[86:89], v[62:65]
	v_mfma_f32_16x16x32_bf16 v[62:65], v[78:81], v[94:97], v[30:33]
	v_mfma_f32_16x16x32_bf16 v[30:33], v[78:81], v[98:101], v[70:73]
	v_add_f32_e64 v66, v66, v68
	v_add_f32_e64 v67, v67, v69
	v_pk_add_f32 v[68:69], v[114:115], v[114:115] op_sel:[0,1] op_sel_hi:[1,0]
	v_pk_add_f32 v[66:67], v[66:67], v[66:67] op_sel:[0,1] op_sel_hi:[1,0]
	v_add_f32_e32 v74, v116, v117
	v_add_f32_e32 v76, v118, v119
	v_mov_b32_e32 v69, v120
	v_mov_b32_e32 v67, v121
	v_pk_add_f32 v[66:67], v[68:69], v[66:67]
	v_pk_add_f32 v[68:69], v[74:75], v[76:77]
	s_nop 0
	v_pk_add_f32 v[66:67], v[66:67], v[68:69]
	s_nop 0
	v_add_f32_e32 v66, v66, v67
	s_setprio 0
	ds_bpermute_b32 v67, v177, v66
	ds_bpermute_b32 v68, v177, v122
	v_mov_b32_e32 v70, v185
	s_waitcnt lgkmcnt(1)
	v_add_f32_e32 v66, v66, v67
	s_waitcnt lgkmcnt(0)
	v_add_f32_e32 v67, v122, v68
	ds_bpermute_b32 v68, v188, v66
	ds_bpermute_b32 v69, v188, v67
	s_waitcnt lgkmcnt(1)
	v_add_f32_e32 v66, v66, v68
	s_waitcnt lgkmcnt(0)
	v_add_f32_e32 v67, v67, v69
	v_rcp_f32_e32 v68, v66
	v_rcp_f32_e32 v66, v67
	v_mov_b32_e32 v67, v176
	v_mov_b32_e32 v69, v180
	s_branch .LBB0_641
